# grid barrier v2: every XCD leader adds to all per-XCD generation words after its L2 writeback (no cross-XCD counter round trip); pollers wait for the full count
# baseline (speedup 1.0000x reference)
; __device__ __forceinline__ unsigned xb_ld(unsigned* p)              { return __hip_atomic_load(p, __ATOMIC_RELAXED, __HIP_MEMORY_SCOPE_AGENT); }
; __device__ __forceinline__ unsigned xb_add(unsigned* p, unsigned v) { return __hip_atomic_fetch_add(p, v, __ATOMIC_RELAXED, __HIP_MEMORY_SCOPE_AGENT); }
; #define XB_SPIN(cond, bar) do { unsigned _sp = 0; while (cond) { __builtin_amdgcn_s_sleep(1); \
;     if ((++_sp & 255u) == 0u) { if (xb_ld(&(bar)[XB_TMO])) break; if (_sp > XB_SPIN_CAP) { atomicAdd(&(bar)[XB_TMO], 1u); break; } } } } while (0)
; __device__ __forceinline__ void xcd_barrier(const XcdBarrier& b) {
;     ...
;         const unsigned old = xb_add(&bar[XB_XSUB(b.x)], 1u);
;         const unsigned gen = old / nloc;
;         if (old + 1u == (gen + 1u) * nloc) {
;             asm volatile("buffer_inv sc1" ::: "memory");
;             __builtin_amdgcn_fence(__ATOMIC_RELEASE, "agent");
;             asm volatile("s_waitcnt vmcnt(0)" ::: "memory");
;             const unsigned og = xb_add(&bar[XB_TOP], 1u);
;             const unsigned tg = og / nx;
;             if (og + 1u == (tg + 1u) * nx) xb_add(&bar[XB_TOPGEN], 1u);
;             else XB_SPIN(xb_ld(&bar[XB_TOPGEN]) == tg, bar);
;             asm volatile("" ::: "memory");
;             xb_add(&bar[XB_XGEN(b.x)], 1u);
;             asm volatile("" ::: "memory");
;         } else {
;             asm volatile("buffer_inv sc1" ::: "memory");
;             XB_SPIN(xb_ld(&bar[XB_XGEN(b.x)]) == gen, bar);
;             asm volatile("" ::: "memory");
;             asm volatile("s_waitcnt vmcnt(0)" ::: "memory");
;         }
.LBB0_33:
	s_or_b64 exec, exec, s[10:11]
	v_cvt_f32_u32_e32 v5, v3
	s_waitcnt vmcnt(0)
	v_readfirstlane_b32 s0, v4
	v_sub_u32_e32 v4, 0, v3
	v_rcp_iflag_f32_e32 v5, v5
	v_add_u32_e32 v6, s0, v2
	v_mul_f32_e32 v5, 0x4f7ffffe, v5
	v_cvt_u32_f32_e32 v5, v5
	v_mul_lo_u32 v2, v4, v5
	v_mul_hi_u32 v2, v5, v2
	v_add_u32_e32 v2, v5, v2
	v_mul_hi_u32 v2, v6, v2
	v_mul_lo_u32 v4, v2, v3
	v_sub_u32_e32 v4, v6, v4
	v_add_u32_e32 v5, 1, v2
	v_cmp_ge_u32_e32 vcc, v4, v3
	s_nop 1
	v_cndmask_b32_e32 v2, v2, v5, vcc
	v_sub_u32_e32 v5, v4, v3
	v_cndmask_b32_e32 v4, v4, v5, vcc
	v_add_u32_e32 v5, 1, v2
	v_cmp_ge_u32_e32 vcc, v4, v3
	v_add_u32_e32 v4, 1, v6
	s_nop 0
	v_cndmask_b32_e32 v2, v2, v5, vcc
	v_mul_lo_u32 v5, v3, v2
	v_add_u32_e32 v7, 1, v2
	v_mul_lo_u32 v7, v7, v1
	v_add_u32_e32 v7, v7, v2
	v_add_u32_e32 v3, v5, v3
	v_readfirstlane_b32 s98, v7
	v_cmp_ne_u32_e32 vcc, v4, v3
	s_and_saveexec_b64 s[0:1], vcc
	s_xor_b64 s[0:1], exec, s[0:1]
	s_cbranch_execz .LBB0_47
	buffer_inv sc1
	v_mov_b32_e32 v2, s98
	s_waitcnt lgkmcnt(0)
	v_mov_b32_e32 v1, 0x2000
	global_load_dword v1, v1, s[4:5] offset:1024 sc1
	s_add_u32 s14, s4, 0x2400
	s_addc_u32 s15, s5, 0
	s_waitcnt vmcnt(0)
	v_cmp_lt_u32_e32 vcc, v1, v2
	s_and_saveexec_b64 s[10:11], vcc
	s_cbranch_execz .LBB0_46
	s_add_u32 s12, s82, 0x4200
	s_addc_u32 s13, s83, 0
	s_mov_b32 s3, 1
	s_mov_b64 s[16:17], 0
	v_mov_b32_e32 v1, 0
	s_branch .LBB0_37

; __device__ __forceinline__ unsigned xb_ld(unsigned* p)              { return __hip_atomic_load(p, __ATOMIC_RELAXED, __HIP_MEMORY_SCOPE_AGENT); }
; __device__ __forceinline__ unsigned xb_add(unsigned* p, unsigned v) { return __hip_atomic_fetch_add(p, v, __ATOMIC_RELAXED, __HIP_MEMORY_SCOPE_AGENT); }
; #define XB_SPIN(cond, bar) do { unsigned _sp = 0; while (cond) { __builtin_amdgcn_s_sleep(1); \
;     if ((++_sp & 255u) == 0u) { if (xb_ld(&(bar)[XB_TMO])) break; if (_sp > XB_SPIN_CAP) { atomicAdd(&(bar)[XB_TMO], 1u); break; } } } } while (0)
; __device__ __forceinline__ void xcd_barrier(const XcdBarrier& b) {
;     ...
;             asm volatile("buffer_inv sc1" ::: "memory");
;             __builtin_amdgcn_fence(__ATOMIC_RELEASE, "agent");
;             asm volatile("s_waitcnt vmcnt(0)" ::: "memory");
;             const unsigned og = xb_add(&bar[XB_TOP], 1u);
;             const unsigned tg = og / nx;
;             if (og + 1u == (tg + 1u) * nx) xb_add(&bar[XB_TOPGEN], 1u);
;             else XB_SPIN(xb_ld(&bar[XB_TOPGEN]) == tg, bar);
;             asm volatile("" ::: "memory");
;             xb_add(&bar[XB_XGEN(b.x)], 1u);
;             asm volatile("" ::: "memory");
.LBB0_47:
	s_andn2_saveexec_b64 s[0:1], s[0:1]
	s_cbranch_execz .LBB0_67
	s_mov_b64 s[0:1], exec
	buffer_inv sc1
	buffer_wbl2 sc1
	s_waitcnt vmcnt(0) lgkmcnt(0)
	s_waitcnt vmcnt(0)
	v_mbcnt_lo_u32_b32 v2, s0, 0
	v_mbcnt_hi_u32_b32 v2, s1, v2
	v_cmp_eq_u32_e32 vcc, 0, v2
	s_and_saveexec_b64 s[10:11], vcc
	s_cbranch_execz .LBB0_50
	s_bcnt1_i32_b64 s0, s[0:1]
	v_mov_b32_e32 v3, 0x7000
	v_mov_b32_e32 v4, s0
	v_mov_b32_e32 v3, 0x6400
	global_atomic_add v3, v4, s[82:83]
	global_atomic_add v3, v4, s[82:83] offset:256
	global_atomic_add v3, v4, s[82:83] offset:512
	global_atomic_add v3, v4, s[82:83] offset:768
	global_atomic_add v3, v4, s[82:83] offset:1024
	global_atomic_add v3, v4, s[82:83] offset:1280
	global_atomic_add v3, v4, s[82:83] offset:1536
	global_atomic_add v3, v4, s[82:83] offset:1792
	global_atomic_add v3, v4, s[82:83] offset:2048
	global_atomic_add v3, v4, s[82:83] offset:2304
	global_atomic_add v3, v4, s[82:83] offset:2560
	global_atomic_add v3, v4, s[82:83] offset:2816
	global_atomic_add v3, v4, s[82:83] offset:3072
	global_atomic_add v3, v4, s[82:83] offset:3328
	global_atomic_add v3, v4, s[82:83] offset:3584
	global_atomic_add v3, v4, s[82:83] offset:3840
.LBB0_50:
	s_or_b64 exec, exec, s[10:11]
	v_cvt_f32_u32_e32 v4, v1
	s_nop 0
	v_readfirstlane_b32 s0, v3
	s_add_u32 s10, s82, 0x7500
	s_addc_u32 s11, s83, 0
	v_rcp_iflag_f32_e32 v4, v4
	v_add_u32_e32 v2, s0, v2
	v_add_u32_e32 v5, 1, v2
	s_mov_b64 s[12:13], -1
	v_mul_f32_e32 v3, 0x4f7ffffe, v4
	v_cvt_u32_f32_e32 v3, v3
	v_sub_u32_e32 v4, 0, v1
	v_mul_lo_u32 v4, v4, v3
	v_mul_hi_u32 v4, v3, v4
	v_add_u32_e32 v3, v3, v4
	v_mul_hi_u32 v3, v2, v3
	v_mul_lo_u32 v4, v3, v1
	v_sub_u32_e32 v2, v2, v4
	v_add_u32_e32 v6, 1, v3
	v_cmp_ge_u32_e32 vcc, v2, v1
	v_sub_u32_e32 v4, v2, v1
	s_nop 0
	v_cndmask_b32_e32 v3, v3, v6, vcc
	v_cndmask_b32_e32 v2, v2, v4, vcc
	v_add_u32_e32 v4, 1, v3
	v_cmp_ge_u32_e32 vcc, v2, v1
	s_nop 1
	v_cndmask_b32_e32 v4, v3, v4, vcc
	v_mul_lo_u32 v2, v1, v4
	v_add_u32_e32 v1, v2, v1
	s_mov_b64 vcc, exec
	v_mov_b64_e32 v[2:3], s[10:11]
	s_and_saveexec_b64 s[0:1], vcc
	s_cbranch_execz .LBB0_62
	s_add_u32 s10, s4, 0x2400
	s_addc_u32 s11, s5, 0
	v_mov_b32_e32 v4, s98
	v_mov_b32_e32 v1, 0
	global_load_dword v2, v1, s[10:11] sc1
	s_mov_b64 s[16:17], 0
	s_waitcnt vmcnt(0)
	v_cmp_lt_u32_e32 vcc, v2, v4
	s_and_saveexec_b64 s[14:15], vcc
	s_cbranch_execz .LBB0_61
	s_add_u32 s12, s82, 0x4200
	s_addc_u32 s13, s83, 0
	s_mov_b32 s3, 1
	s_branch .LBB0_54

; __device__ __forceinline__ unsigned xb_ld(unsigned* p)              { return __hip_atomic_load(p, __ATOMIC_RELAXED, __HIP_MEMORY_SCOPE_AGENT); }
; __device__ __forceinline__ unsigned xb_add(unsigned* p, unsigned v) { return __hip_atomic_fetch_add(p, v, __ATOMIC_RELAXED, __HIP_MEMORY_SCOPE_AGENT); }
; #define XB_SPIN(cond, bar) do { unsigned _sp = 0; while (cond) { __builtin_amdgcn_s_sleep(1); \
;     if ((++_sp & 255u) == 0u) { if (xb_ld(&(bar)[XB_TMO])) break; if (_sp > XB_SPIN_CAP) { atomicAdd(&(bar)[XB_TMO], 1u); break; } } } } while (0)
; __device__ __forceinline__ void xcd_barrier(const XcdBarrier& b) {
;     ...
;         const unsigned old = xb_add(&bar[XB_XSUB(b.x)], 1u);
;         const unsigned gen = old / nloc;
;         if (old + 1u == (gen + 1u) * nloc) {
;             asm volatile("buffer_inv sc1" ::: "memory");
;             __builtin_amdgcn_fence(__ATOMIC_RELEASE, "agent");
;             asm volatile("s_waitcnt vmcnt(0)" ::: "memory");
;             const unsigned og = xb_add(&bar[XB_TOP], 1u);
;             const unsigned tg = og / nx;
;             if (og + 1u == (tg + 1u) * nx) xb_add(&bar[XB_TOPGEN], 1u);
;             else XB_SPIN(xb_ld(&bar[XB_TOPGEN]) == tg, bar);
;             asm volatile("" ::: "memory");
;             xb_add(&bar[XB_XGEN(b.x)], 1u);
;             asm volatile("" ::: "memory");
;         } else {
;             asm volatile("buffer_inv sc1" ::: "memory");
;             XB_SPIN(xb_ld(&bar[XB_XGEN(b.x)]) == gen, bar);
;             asm volatile("" ::: "memory");
;             asm volatile("s_waitcnt vmcnt(0)" ::: "memory");
;         }
.LBB0_103:
	s_or_b64 exec, exec, s[10:11]
	v_cvt_f32_u32_e32 v5, v3
	s_waitcnt vmcnt(0)
	v_readfirstlane_b32 s3, v4
	v_sub_u32_e32 v4, 0, v3
	v_rcp_iflag_f32_e32 v5, v5
	v_add_u32_e32 v6, s3, v2
	v_mul_f32_e32 v5, 0x4f7ffffe, v5
	v_cvt_u32_f32_e32 v5, v5
	v_mul_lo_u32 v2, v4, v5
	v_mul_hi_u32 v2, v5, v2
	v_add_u32_e32 v2, v5, v2
	v_mul_hi_u32 v2, v6, v2
	v_mul_lo_u32 v4, v2, v3
	v_sub_u32_e32 v4, v6, v4
	v_add_u32_e32 v5, 1, v2
	v_cmp_ge_u32_e32 vcc, v4, v3
	s_nop 1
	v_cndmask_b32_e32 v2, v2, v5, vcc
	v_sub_u32_e32 v5, v4, v3
	v_cndmask_b32_e32 v4, v4, v5, vcc
	v_add_u32_e32 v5, 1, v2
	v_cmp_ge_u32_e32 vcc, v4, v3
	v_add_u32_e32 v4, 1, v6
	s_nop 0
	v_cndmask_b32_e32 v2, v2, v5, vcc
	v_mul_lo_u32 v5, v3, v2
	v_add_u32_e32 v7, 1, v2
	v_mul_lo_u32 v7, v7, v1
	v_add_u32_e32 v7, v7, v2
	v_add_u32_e32 v3, v5, v3
	v_readfirstlane_b32 s98, v7
	v_cmp_ne_u32_e32 vcc, v4, v3
	s_and_saveexec_b64 s[8:9], vcc
	s_xor_b64 s[8:9], exec, s[8:9]
	s_cbranch_execz .LBB0_117
	buffer_inv sc1
	v_mov_b32_e32 v2, s98
	s_waitcnt lgkmcnt(0)
	v_mov_b32_e32 v1, 0x2000
	global_load_dword v1, v1, s[4:5] offset:1024 sc1
	s_add_u32 s14, s4, 0x2400
	s_addc_u32 s15, s5, 0
	s_waitcnt vmcnt(0)
	v_cmp_lt_u32_e32 vcc, v1, v2
	s_and_saveexec_b64 s[10:11], vcc
	s_cbranch_execz .LBB0_116
	s_add_u32 s12, s82, 0x4200
	s_addc_u32 s13, s83, 0
	s_mov_b32 s3, 1
	s_mov_b64 s[16:17], 0
	v_mov_b32_e32 v1, 0
	s_branch .LBB0_107

; __device__ __forceinline__ unsigned xb_ld(unsigned* p)              { return __hip_atomic_load(p, __ATOMIC_RELAXED, __HIP_MEMORY_SCOPE_AGENT); }
; __device__ __forceinline__ unsigned xb_add(unsigned* p, unsigned v) { return __hip_atomic_fetch_add(p, v, __ATOMIC_RELAXED, __HIP_MEMORY_SCOPE_AGENT); }
; #define XB_SPIN(cond, bar) do { unsigned _sp = 0; while (cond) { __builtin_amdgcn_s_sleep(1); \
;     if ((++_sp & 255u) == 0u) { if (xb_ld(&(bar)[XB_TMO])) break; if (_sp > XB_SPIN_CAP) { atomicAdd(&(bar)[XB_TMO], 1u); break; } } } } while (0)
; __device__ __forceinline__ void xcd_barrier(const XcdBarrier& b) {
;     ...
;             asm volatile("buffer_inv sc1" ::: "memory");
;             __builtin_amdgcn_fence(__ATOMIC_RELEASE, "agent");
;             asm volatile("s_waitcnt vmcnt(0)" ::: "memory");
;             const unsigned og = xb_add(&bar[XB_TOP], 1u);
;             const unsigned tg = og / nx;
;             if (og + 1u == (tg + 1u) * nx) xb_add(&bar[XB_TOPGEN], 1u);
;             else XB_SPIN(xb_ld(&bar[XB_TOPGEN]) == tg, bar);
;             asm volatile("" ::: "memory");
;             xb_add(&bar[XB_XGEN(b.x)], 1u);
;             asm volatile("" ::: "memory");
.LBB0_117:
	s_andn2_saveexec_b64 s[8:9], s[8:9]
	s_cbranch_execz .LBB0_137
	s_mov_b64 s[8:9], exec
	buffer_inv sc1
	buffer_wbl2 sc1
	s_waitcnt vmcnt(0) lgkmcnt(0)
	s_waitcnt vmcnt(0)
	v_mbcnt_lo_u32_b32 v2, s8, 0
	v_mbcnt_hi_u32_b32 v2, s9, v2
	v_cmp_eq_u32_e32 vcc, 0, v2
	s_and_saveexec_b64 s[10:11], vcc
	s_cbranch_execz .LBB0_120
	s_bcnt1_i32_b64 s3, s[8:9]
	v_mov_b32_e32 v3, 0x7000
	v_mov_b32_e32 v4, s3
	v_mov_b32_e32 v3, 0x6400
	global_atomic_add v3, v4, s[82:83]
	global_atomic_add v3, v4, s[82:83] offset:256
	global_atomic_add v3, v4, s[82:83] offset:512
	global_atomic_add v3, v4, s[82:83] offset:768
	global_atomic_add v3, v4, s[82:83] offset:1024
	global_atomic_add v3, v4, s[82:83] offset:1280
	global_atomic_add v3, v4, s[82:83] offset:1536
	global_atomic_add v3, v4, s[82:83] offset:1792
	global_atomic_add v3, v4, s[82:83] offset:2048
	global_atomic_add v3, v4, s[82:83] offset:2304
	global_atomic_add v3, v4, s[82:83] offset:2560
	global_atomic_add v3, v4, s[82:83] offset:2816
	global_atomic_add v3, v4, s[82:83] offset:3072
	global_atomic_add v3, v4, s[82:83] offset:3328
	global_atomic_add v3, v4, s[82:83] offset:3584
	global_atomic_add v3, v4, s[82:83] offset:3840
.LBB0_120:
	s_or_b64 exec, exec, s[10:11]
	v_cvt_f32_u32_e32 v4, v1
	s_nop 0
	v_readfirstlane_b32 s3, v3
	s_add_u32 s10, s82, 0x7500
	s_addc_u32 s11, s83, 0
	v_rcp_iflag_f32_e32 v4, v4
	v_add_u32_e32 v2, s3, v2
	v_add_u32_e32 v5, 1, v2
	s_mov_b64 s[12:13], -1
	v_mul_f32_e32 v3, 0x4f7ffffe, v4
	v_cvt_u32_f32_e32 v3, v3
	v_sub_u32_e32 v4, 0, v1
	v_mul_lo_u32 v4, v4, v3
	v_mul_hi_u32 v4, v3, v4
	v_add_u32_e32 v3, v3, v4
	v_mul_hi_u32 v3, v2, v3
	v_mul_lo_u32 v4, v3, v1
	v_sub_u32_e32 v2, v2, v4
	v_add_u32_e32 v6, 1, v3
	v_cmp_ge_u32_e32 vcc, v2, v1
	v_sub_u32_e32 v4, v2, v1
	s_nop 0
	v_cndmask_b32_e32 v3, v3, v6, vcc
	v_cndmask_b32_e32 v2, v2, v4, vcc
	v_add_u32_e32 v4, 1, v3
	v_cmp_ge_u32_e32 vcc, v2, v1
	s_nop 1
	v_cndmask_b32_e32 v4, v3, v4, vcc
	v_mul_lo_u32 v2, v1, v4
	v_add_u32_e32 v1, v2, v1
	s_mov_b64 vcc, exec
	v_mov_b64_e32 v[2:3], s[10:11]
	s_and_saveexec_b64 s[8:9], vcc
	s_cbranch_execz .LBB0_132
	s_add_u32 s10, s4, 0x2400
	s_addc_u32 s11, s5, 0
	v_mov_b32_e32 v4, s98
	v_mov_b32_e32 v1, 0
	global_load_dword v2, v1, s[10:11] sc1
	s_mov_b64 s[16:17], 0
	s_waitcnt vmcnt(0)
	v_cmp_lt_u32_e32 vcc, v2, v4
	s_and_saveexec_b64 s[14:15], vcc
	s_cbranch_execz .LBB0_131
	s_add_u32 s12, s82, 0x4200
	s_addc_u32 s13, s83, 0
	s_mov_b32 s3, 1
	s_branch .LBB0_124

; __device__ __forceinline__ unsigned xb_ld(unsigned* p)              { return __hip_atomic_load(p, __ATOMIC_RELAXED, __HIP_MEMORY_SCOPE_AGENT); }
; __device__ __forceinline__ unsigned xb_add(unsigned* p, unsigned v) { return __hip_atomic_fetch_add(p, v, __ATOMIC_RELAXED, __HIP_MEMORY_SCOPE_AGENT); }
; #define XB_SPIN(cond, bar) do { unsigned _sp = 0; while (cond) { __builtin_amdgcn_s_sleep(1); \
;     if ((++_sp & 255u) == 0u) { if (xb_ld(&(bar)[XB_TMO])) break; if (_sp > XB_SPIN_CAP) { atomicAdd(&(bar)[XB_TMO], 1u); break; } } } } while (0)
; __device__ __forceinline__ void xcd_barrier(const XcdBarrier& b) {
;     ...
;         const unsigned old = xb_add(&bar[XB_XSUB(b.x)], 1u);
;         const unsigned gen = old / nloc;
;         if (old + 1u == (gen + 1u) * nloc) {
;             asm volatile("buffer_inv sc1" ::: "memory");
;             __builtin_amdgcn_fence(__ATOMIC_RELEASE, "agent");
;             asm volatile("s_waitcnt vmcnt(0)" ::: "memory");
;             const unsigned og = xb_add(&bar[XB_TOP], 1u);
;             const unsigned tg = og / nx;
;             if (og + 1u == (tg + 1u) * nx) xb_add(&bar[XB_TOPGEN], 1u);
;             else XB_SPIN(xb_ld(&bar[XB_TOPGEN]) == tg, bar);
;             asm volatile("" ::: "memory");
;             xb_add(&bar[XB_XGEN(b.x)], 1u);
;             asm volatile("" ::: "memory");
;         } else {
;             asm volatile("buffer_inv sc1" ::: "memory");
;             XB_SPIN(xb_ld(&bar[XB_XGEN(b.x)]) == gen, bar);
;             asm volatile("" ::: "memory");
;             asm volatile("s_waitcnt vmcnt(0)" ::: "memory");
;         }
.LBB0_183:
	s_or_b64 exec, exec, s[10:11]
	v_cvt_f32_u32_e32 v5, v3
	s_waitcnt vmcnt(0)
	v_readfirstlane_b32 s8, v4
	v_sub_u32_e32 v4, 0, v3
	v_rcp_iflag_f32_e32 v5, v5
	v_add_u32_e32 v6, s8, v2
	v_mul_f32_e32 v5, 0x4f7ffffe, v5
	v_cvt_u32_f32_e32 v5, v5
	v_mul_lo_u32 v2, v4, v5
	v_mul_hi_u32 v2, v5, v2
	v_add_u32_e32 v2, v5, v2
	v_mul_hi_u32 v2, v6, v2
	v_mul_lo_u32 v4, v2, v3
	v_sub_u32_e32 v4, v6, v4
	v_add_u32_e32 v5, 1, v2
	v_cmp_ge_u32_e32 vcc, v4, v3
	s_nop 1
	v_cndmask_b32_e32 v2, v2, v5, vcc
	v_sub_u32_e32 v5, v4, v3
	v_cndmask_b32_e32 v4, v4, v5, vcc
	v_add_u32_e32 v5, 1, v2
	v_cmp_ge_u32_e32 vcc, v4, v3
	v_add_u32_e32 v4, 1, v6
	s_nop 0
	v_cndmask_b32_e32 v2, v2, v5, vcc
	v_mul_lo_u32 v5, v3, v2
	v_add_u32_e32 v7, 1, v2
	v_mul_lo_u32 v7, v7, v1
	v_add_u32_e32 v7, v7, v2
	v_add_u32_e32 v3, v5, v3
	v_readfirstlane_b32 s98, v7
	v_cmp_ne_u32_e32 vcc, v4, v3
	s_and_saveexec_b64 s[8:9], vcc
	s_xor_b64 s[8:9], exec, s[8:9]
	s_cbranch_execz .LBB0_197
	buffer_inv sc1
	v_mov_b32_e32 v2, s98
	s_waitcnt lgkmcnt(0)
	v_mov_b32_e32 v1, 0x2000
	global_load_dword v1, v1, s[4:5] offset:1024 sc1
	s_add_u32 s16, s4, 0x2400
	s_addc_u32 s17, s5, 0
	s_waitcnt vmcnt(0)
	v_cmp_lt_u32_e32 vcc, v1, v2
	s_and_saveexec_b64 s[10:11], vcc
	s_cbranch_execz .LBB0_196
	s_add_u32 s14, s82, 0x4200
	s_addc_u32 s15, s83, 0
	s_mov_b32 s28, 1
	s_mov_b64 s[18:19], 0
	v_mov_b32_e32 v1, 0
	s_branch .LBB0_187

; __device__ __forceinline__ unsigned xb_ld(unsigned* p)              { return __hip_atomic_load(p, __ATOMIC_RELAXED, __HIP_MEMORY_SCOPE_AGENT); }
; __device__ __forceinline__ unsigned xb_add(unsigned* p, unsigned v) { return __hip_atomic_fetch_add(p, v, __ATOMIC_RELAXED, __HIP_MEMORY_SCOPE_AGENT); }
; #define XB_SPIN(cond, bar) do { unsigned _sp = 0; while (cond) { __builtin_amdgcn_s_sleep(1); \
;     if ((++_sp & 255u) == 0u) { if (xb_ld(&(bar)[XB_TMO])) break; if (_sp > XB_SPIN_CAP) { atomicAdd(&(bar)[XB_TMO], 1u); break; } } } } while (0)
; __device__ __forceinline__ void xcd_barrier(const XcdBarrier& b) {
;     ...
;             asm volatile("buffer_inv sc1" ::: "memory");
;             __builtin_amdgcn_fence(__ATOMIC_RELEASE, "agent");
;             asm volatile("s_waitcnt vmcnt(0)" ::: "memory");
;             const unsigned og = xb_add(&bar[XB_TOP], 1u);
;             const unsigned tg = og / nx;
;             if (og + 1u == (tg + 1u) * nx) xb_add(&bar[XB_TOPGEN], 1u);
;             else XB_SPIN(xb_ld(&bar[XB_TOPGEN]) == tg, bar);
;             asm volatile("" ::: "memory");
;             xb_add(&bar[XB_XGEN(b.x)], 1u);
;             asm volatile("" ::: "memory");
.LBB0_197:
	s_andn2_saveexec_b64 s[8:9], s[8:9]
	s_cbranch_execz .LBB0_217
	s_mov_b64 s[8:9], exec
	buffer_inv sc1
	buffer_wbl2 sc1
	s_waitcnt vmcnt(0) lgkmcnt(0)
	s_waitcnt vmcnt(0)
	v_mbcnt_lo_u32_b32 v2, s8, 0
	v_mbcnt_hi_u32_b32 v2, s9, v2
	v_cmp_eq_u32_e32 vcc, 0, v2
	s_and_saveexec_b64 s[10:11], vcc
	s_cbranch_execz .LBB0_200
	s_bcnt1_i32_b64 s8, s[8:9]
	v_mov_b32_e32 v3, 0x7000
	v_mov_b32_e32 v4, s8
	v_mov_b32_e32 v3, 0x6400
	global_atomic_add v3, v4, s[82:83]
	global_atomic_add v3, v4, s[82:83] offset:256
	global_atomic_add v3, v4, s[82:83] offset:512
	global_atomic_add v3, v4, s[82:83] offset:768
	global_atomic_add v3, v4, s[82:83] offset:1024
	global_atomic_add v3, v4, s[82:83] offset:1280
	global_atomic_add v3, v4, s[82:83] offset:1536
	global_atomic_add v3, v4, s[82:83] offset:1792
	global_atomic_add v3, v4, s[82:83] offset:2048
	global_atomic_add v3, v4, s[82:83] offset:2304
	global_atomic_add v3, v4, s[82:83] offset:2560
	global_atomic_add v3, v4, s[82:83] offset:2816
	global_atomic_add v3, v4, s[82:83] offset:3072
	global_atomic_add v3, v4, s[82:83] offset:3328
	global_atomic_add v3, v4, s[82:83] offset:3584
	global_atomic_add v3, v4, s[82:83] offset:3840
.LBB0_200:
	s_or_b64 exec, exec, s[10:11]
	v_cvt_f32_u32_e32 v4, v1
	s_nop 0
	v_readfirstlane_b32 s8, v3
	s_add_u32 s10, s82, 0x7500
	s_addc_u32 s11, s83, 0
	v_rcp_iflag_f32_e32 v4, v4
	v_add_u32_e32 v2, s8, v2
	v_add_u32_e32 v5, 1, v2
	s_mov_b64 s[14:15], -1
	v_mul_f32_e32 v3, 0x4f7ffffe, v4
	v_cvt_u32_f32_e32 v3, v3
	v_sub_u32_e32 v4, 0, v1
	v_mul_lo_u32 v4, v4, v3
	v_mul_hi_u32 v4, v3, v4
	v_add_u32_e32 v3, v3, v4
	v_mul_hi_u32 v3, v2, v3
	v_mul_lo_u32 v4, v3, v1
	v_sub_u32_e32 v2, v2, v4
	v_add_u32_e32 v6, 1, v3
	v_cmp_ge_u32_e32 vcc, v2, v1
	v_sub_u32_e32 v4, v2, v1
	s_nop 0
	v_cndmask_b32_e32 v3, v3, v6, vcc
	v_cndmask_b32_e32 v2, v2, v4, vcc
	v_add_u32_e32 v4, 1, v3
	v_cmp_ge_u32_e32 vcc, v2, v1
	s_nop 1
	v_cndmask_b32_e32 v4, v3, v4, vcc
	v_mul_lo_u32 v2, v1, v4
	v_add_u32_e32 v1, v2, v1
	s_mov_b64 vcc, exec
	v_mov_b64_e32 v[2:3], s[10:11]
	s_and_saveexec_b64 s[8:9], vcc
	s_cbranch_execz .LBB0_212
	s_add_u32 s10, s4, 0x2400
	s_addc_u32 s11, s5, 0
	v_mov_b32_e32 v4, s98
	v_mov_b32_e32 v1, 0
	global_load_dword v2, v1, s[10:11] sc1
	s_mov_b64 s[18:19], 0
	s_waitcnt vmcnt(0)
	v_cmp_lt_u32_e32 vcc, v2, v4
	s_and_saveexec_b64 s[16:17], vcc
	s_cbranch_execz .LBB0_211
	s_add_u32 s14, s82, 0x4200
	s_addc_u32 s15, s83, 0
	s_mov_b32 s28, 1
	s_branch .LBB0_204

; __device__ __forceinline__ unsigned xb_ld(unsigned* p)              { return __hip_atomic_load(p, __ATOMIC_RELAXED, __HIP_MEMORY_SCOPE_AGENT); }
; __device__ __forceinline__ unsigned xb_add(unsigned* p, unsigned v) { return __hip_atomic_fetch_add(p, v, __ATOMIC_RELAXED, __HIP_MEMORY_SCOPE_AGENT); }
; #define XB_SPIN(cond, bar) do { unsigned _sp = 0; while (cond) { __builtin_amdgcn_s_sleep(1); \
;     if ((++_sp & 255u) == 0u) { if (xb_ld(&(bar)[XB_TMO])) break; if (_sp > XB_SPIN_CAP) { atomicAdd(&(bar)[XB_TMO], 1u); break; } } } } while (0)
; __device__ __forceinline__ void xcd_barrier(const XcdBarrier& b) {
;     ...
;         const unsigned old = xb_add(&bar[XB_XSUB(b.x)], 1u);
;         const unsigned gen = old / nloc;
;         if (old + 1u == (gen + 1u) * nloc) {
;             asm volatile("buffer_inv sc1" ::: "memory");
;             __builtin_amdgcn_fence(__ATOMIC_RELEASE, "agent");
;             asm volatile("s_waitcnt vmcnt(0)" ::: "memory");
;             const unsigned og = xb_add(&bar[XB_TOP], 1u);
;             const unsigned tg = og / nx;
;             if (og + 1u == (tg + 1u) * nx) xb_add(&bar[XB_TOPGEN], 1u);
;             else XB_SPIN(xb_ld(&bar[XB_TOPGEN]) == tg, bar);
;             asm volatile("" ::: "memory");
;             xb_add(&bar[XB_XGEN(b.x)], 1u);
;             asm volatile("" ::: "memory");
;         } else {
;             asm volatile("buffer_inv sc1" ::: "memory");
;             XB_SPIN(xb_ld(&bar[XB_XGEN(b.x)]) == gen, bar);
;             asm volatile("" ::: "memory");
;             asm volatile("s_waitcnt vmcnt(0)" ::: "memory");
;         }
.LBB0_626:
	s_or_b64 exec, exec, s[10:11]
	v_cvt_f32_u32_e32 v5, v3
	s_waitcnt vmcnt(0)
	v_readfirstlane_b32 s8, v4
	v_sub_u32_e32 v4, 0, v3
	v_rcp_iflag_f32_e32 v5, v5
	v_add_u32_e32 v6, s8, v2
	v_mul_f32_e32 v5, 0x4f7ffffe, v5
	v_cvt_u32_f32_e32 v5, v5
	v_mul_lo_u32 v2, v4, v5
	v_mul_hi_u32 v2, v5, v2
	v_add_u32_e32 v2, v5, v2
	v_mul_hi_u32 v2, v6, v2
	v_mul_lo_u32 v4, v2, v3
	v_sub_u32_e32 v4, v6, v4
	v_add_u32_e32 v5, 1, v2
	v_cmp_ge_u32_e32 vcc, v4, v3
	s_nop 1
	v_cndmask_b32_e32 v2, v2, v5, vcc
	v_sub_u32_e32 v5, v4, v3
	v_cndmask_b32_e32 v4, v4, v5, vcc
	v_add_u32_e32 v5, 1, v2
	v_cmp_ge_u32_e32 vcc, v4, v3
	v_add_u32_e32 v4, 1, v6
	s_nop 0
	v_cndmask_b32_e32 v2, v2, v5, vcc
	v_mul_lo_u32 v5, v3, v2
	v_add_u32_e32 v7, 1, v2
	v_mul_lo_u32 v7, v7, v1
	v_add_u32_e32 v7, v7, v2
	v_add_u32_e32 v3, v5, v3
	v_readfirstlane_b32 s98, v7
	v_cmp_ne_u32_e32 vcc, v4, v3
	s_and_saveexec_b64 s[8:9], vcc
	s_xor_b64 s[8:9], exec, s[8:9]
	s_cbranch_execz .LBB0_640
	buffer_inv sc1
	v_mov_b32_e32 v2, s98
	s_waitcnt lgkmcnt(0)
	v_mov_b32_e32 v1, 0x2000
	global_load_dword v1, v1, s[6:7] offset:1024 sc1
	s_add_u32 s14, s6, 0x2400
	s_addc_u32 s15, s7, 0
	s_waitcnt vmcnt(0)
	v_cmp_lt_u32_e32 vcc, v1, v2
	s_and_saveexec_b64 s[10:11], vcc
	s_cbranch_execz .LBB0_639
	s_add_u32 s12, s82, 0x4200
	s_addc_u32 s13, s83, 0
	s_mov_b32 s26, 1
	s_mov_b64 s[16:17], 0
	v_mov_b32_e32 v1, 0
	s_branch .LBB0_630

; __device__ __forceinline__ unsigned xb_ld(unsigned* p)              { return __hip_atomic_load(p, __ATOMIC_RELAXED, __HIP_MEMORY_SCOPE_AGENT); }
; __device__ __forceinline__ unsigned xb_add(unsigned* p, unsigned v) { return __hip_atomic_fetch_add(p, v, __ATOMIC_RELAXED, __HIP_MEMORY_SCOPE_AGENT); }
; #define XB_SPIN(cond, bar) do { unsigned _sp = 0; while (cond) { __builtin_amdgcn_s_sleep(1); \
;     if ((++_sp & 255u) == 0u) { if (xb_ld(&(bar)[XB_TMO])) break; if (_sp > XB_SPIN_CAP) { atomicAdd(&(bar)[XB_TMO], 1u); break; } } } } while (0)
; __device__ __forceinline__ void xcd_barrier(const XcdBarrier& b) {
;     ...
;             asm volatile("buffer_inv sc1" ::: "memory");
;             __builtin_amdgcn_fence(__ATOMIC_RELEASE, "agent");
;             asm volatile("s_waitcnt vmcnt(0)" ::: "memory");
;             const unsigned og = xb_add(&bar[XB_TOP], 1u);
;             const unsigned tg = og / nx;
;             if (og + 1u == (tg + 1u) * nx) xb_add(&bar[XB_TOPGEN], 1u);
;             else XB_SPIN(xb_ld(&bar[XB_TOPGEN]) == tg, bar);
;             asm volatile("" ::: "memory");
;             xb_add(&bar[XB_XGEN(b.x)], 1u);
;             asm volatile("" ::: "memory");
.LBB0_643:
	s_or_b64 exec, exec, s[10:11]
	v_cvt_f32_u32_e32 v4, v1
	s_nop 0
	v_readfirstlane_b32 s8, v3
	s_add_u32 s10, s82, 0x7500
	s_addc_u32 s11, s83, 0
	v_rcp_iflag_f32_e32 v4, v4
	v_add_u32_e32 v2, s8, v2
	v_add_u32_e32 v5, 1, v2
	s_mov_b64 s[12:13], -1
	v_mul_f32_e32 v3, 0x4f7ffffe, v4
	v_cvt_u32_f32_e32 v3, v3
	v_sub_u32_e32 v4, 0, v1
	v_mul_lo_u32 v4, v4, v3
	v_mul_hi_u32 v4, v3, v4
	v_add_u32_e32 v3, v3, v4
	v_mul_hi_u32 v3, v2, v3
	v_mul_lo_u32 v4, v3, v1
	v_sub_u32_e32 v2, v2, v4
	v_add_u32_e32 v6, 1, v3
	v_cmp_ge_u32_e32 vcc, v2, v1
	v_sub_u32_e32 v4, v2, v1
	s_nop 0
	v_cndmask_b32_e32 v3, v3, v6, vcc
	v_cndmask_b32_e32 v2, v2, v4, vcc
	v_add_u32_e32 v4, 1, v3
	v_cmp_ge_u32_e32 vcc, v2, v1
	s_nop 1
	v_cndmask_b32_e32 v4, v3, v4, vcc
	v_mul_lo_u32 v2, v1, v4
	v_add_u32_e32 v1, v2, v1
	s_mov_b64 vcc, exec
	v_mov_b64_e32 v[2:3], s[10:11]
	s_and_saveexec_b64 s[8:9], vcc
	s_cbranch_execz .LBB0_655
	s_add_u32 s10, s6, 0x2400
	s_addc_u32 s11, s7, 0
	v_mov_b32_e32 v4, s98
	v_mov_b32_e32 v1, 0
	global_load_dword v2, v1, s[10:11] sc1
	s_mov_b64 s[16:17], 0
	s_waitcnt vmcnt(0)
	v_cmp_lt_u32_e32 vcc, v2, v4
	s_and_saveexec_b64 s[14:15], vcc
	s_cbranch_execz .LBB0_654
	s_add_u32 s12, s82, 0x4200
	s_addc_u32 s13, s83, 0
	s_mov_b32 s26, 1
	s_branch .LBB0_647

; __device__ __forceinline__ unsigned xb_ld(unsigned* p)              { return __hip_atomic_load(p, __ATOMIC_RELAXED, __HIP_MEMORY_SCOPE_AGENT); }
; __device__ __forceinline__ unsigned xb_add(unsigned* p, unsigned v) { return __hip_atomic_fetch_add(p, v, __ATOMIC_RELAXED, __HIP_MEMORY_SCOPE_AGENT); }
; #define XB_SPIN(cond, bar) do { unsigned _sp = 0; while (cond) { __builtin_amdgcn_s_sleep(1); \
;     if ((++_sp & 255u) == 0u) { if (xb_ld(&(bar)[XB_TMO])) break; if (_sp > XB_SPIN_CAP) { atomicAdd(&(bar)[XB_TMO], 1u); break; } } } } while (0)
; __device__ __forceinline__ void xcd_barrier(const XcdBarrier& b) {
;     ...
;         const unsigned old = xb_add(&bar[XB_XSUB(b.x)], 1u);
;         const unsigned gen = old / nloc;
;         if (old + 1u == (gen + 1u) * nloc) {
;             asm volatile("buffer_inv sc1" ::: "memory");
;             __builtin_amdgcn_fence(__ATOMIC_RELEASE, "agent");
;             asm volatile("s_waitcnt vmcnt(0)" ::: "memory");
;             const unsigned og = xb_add(&bar[XB_TOP], 1u);
;             const unsigned tg = og / nx;
;             if (og + 1u == (tg + 1u) * nx) xb_add(&bar[XB_TOPGEN], 1u);
;             else XB_SPIN(xb_ld(&bar[XB_TOPGEN]) == tg, bar);
;             asm volatile("" ::: "memory");
;             xb_add(&bar[XB_XGEN(b.x)], 1u);
;             asm volatile("" ::: "memory");
;         } else {
;             asm volatile("buffer_inv sc1" ::: "memory");
;             XB_SPIN(xb_ld(&bar[XB_XGEN(b.x)]) == gen, bar);
;             asm volatile("" ::: "memory");
;             asm volatile("s_waitcnt vmcnt(0)" ::: "memory");
;         }
.LBB0_907:
	s_or_b64 exec, exec, s[10:11]
	v_cvt_f32_u32_e32 v5, v3
	s_waitcnt vmcnt(0)
	v_readfirstlane_b32 s8, v4
	v_sub_u32_e32 v4, 0, v3
	v_rcp_iflag_f32_e32 v5, v5
	v_add_u32_e32 v6, s8, v2
	v_mul_f32_e32 v5, 0x4f7ffffe, v5
	v_cvt_u32_f32_e32 v5, v5
	v_mul_lo_u32 v2, v4, v5
	v_mul_hi_u32 v2, v5, v2
	v_add_u32_e32 v2, v5, v2
	v_mul_hi_u32 v2, v6, v2
	v_mul_lo_u32 v4, v2, v3
	v_sub_u32_e32 v4, v6, v4
	v_add_u32_e32 v5, 1, v2
	v_cmp_ge_u32_e32 vcc, v4, v3
	s_nop 1
	v_cndmask_b32_e32 v2, v2, v5, vcc
	v_sub_u32_e32 v5, v4, v3
	v_cndmask_b32_e32 v4, v4, v5, vcc
	v_add_u32_e32 v5, 1, v2
	v_cmp_ge_u32_e32 vcc, v4, v3
	v_add_u32_e32 v4, 1, v6
	s_nop 0
	v_cndmask_b32_e32 v2, v2, v5, vcc
	v_mul_lo_u32 v5, v3, v2
	v_add_u32_e32 v7, 1, v2
	v_mul_lo_u32 v7, v7, v1
	v_add_u32_e32 v7, v7, v2
	v_add_u32_e32 v3, v5, v3
	v_readfirstlane_b32 s98, v7
	v_cmp_ne_u32_e32 vcc, v4, v3
	s_and_saveexec_b64 s[8:9], vcc
	s_xor_b64 s[8:9], exec, s[8:9]
	s_cbranch_execz .LBB0_921
	buffer_inv sc1
	v_mov_b32_e32 v2, s98
	s_waitcnt lgkmcnt(0)
	v_mov_b32_e32 v1, 0x2000
	global_load_dword v1, v1, s[4:5] offset:1024 sc1
	s_add_u32 s14, s4, 0x2400
	s_addc_u32 s15, s5, 0
	s_waitcnt vmcnt(0)
	v_cmp_lt_u32_e32 vcc, v1, v2
	s_and_saveexec_b64 s[10:11], vcc
	s_cbranch_execz .LBB0_920
	s_add_u32 s12, s82, 0x4200
	s_addc_u32 s13, s83, 0
	s_mov_b32 s26, 1
	s_mov_b64 s[16:17], 0
	v_mov_b32_e32 v1, 0
	s_branch .LBB0_911

; __device__ __forceinline__ unsigned xb_ld(unsigned* p)              { return __hip_atomic_load(p, __ATOMIC_RELAXED, __HIP_MEMORY_SCOPE_AGENT); }
; __device__ __forceinline__ unsigned xb_add(unsigned* p, unsigned v) { return __hip_atomic_fetch_add(p, v, __ATOMIC_RELAXED, __HIP_MEMORY_SCOPE_AGENT); }
; #define XB_SPIN(cond, bar) do { unsigned _sp = 0; while (cond) { __builtin_amdgcn_s_sleep(1); \
;     if ((++_sp & 255u) == 0u) { if (xb_ld(&(bar)[XB_TMO])) break; if (_sp > XB_SPIN_CAP) { atomicAdd(&(bar)[XB_TMO], 1u); break; } } } } while (0)
; __device__ __forceinline__ void xcd_barrier(const XcdBarrier& b) {
;     ...
;             asm volatile("buffer_inv sc1" ::: "memory");
;             __builtin_amdgcn_fence(__ATOMIC_RELEASE, "agent");
;             asm volatile("s_waitcnt vmcnt(0)" ::: "memory");
;             const unsigned og = xb_add(&bar[XB_TOP], 1u);
;             const unsigned tg = og / nx;
;             if (og + 1u == (tg + 1u) * nx) xb_add(&bar[XB_TOPGEN], 1u);
;             else XB_SPIN(xb_ld(&bar[XB_TOPGEN]) == tg, bar);
;             asm volatile("" ::: "memory");
;             xb_add(&bar[XB_XGEN(b.x)], 1u);
;             asm volatile("" ::: "memory");
.LBB0_924:
	s_or_b64 exec, exec, s[10:11]
	v_cvt_f32_u32_e32 v4, v1
	s_nop 0
	v_readfirstlane_b32 s8, v3
	s_add_u32 s10, s82, 0x7500
	s_addc_u32 s11, s83, 0
	v_rcp_iflag_f32_e32 v4, v4
	v_add_u32_e32 v2, s8, v2
	v_add_u32_e32 v5, 1, v2
	s_mov_b64 s[12:13], -1
	v_mul_f32_e32 v3, 0x4f7ffffe, v4
	v_cvt_u32_f32_e32 v3, v3
	v_sub_u32_e32 v4, 0, v1
	v_mul_lo_u32 v4, v4, v3
	v_mul_hi_u32 v4, v3, v4
	v_add_u32_e32 v3, v3, v4
	v_mul_hi_u32 v3, v2, v3
	v_mul_lo_u32 v4, v3, v1
	v_sub_u32_e32 v2, v2, v4
	v_add_u32_e32 v6, 1, v3
	v_cmp_ge_u32_e32 vcc, v2, v1
	v_sub_u32_e32 v4, v2, v1
	s_nop 0
	v_cndmask_b32_e32 v3, v3, v6, vcc
	v_cndmask_b32_e32 v2, v2, v4, vcc
	v_add_u32_e32 v4, 1, v3
	v_cmp_ge_u32_e32 vcc, v2, v1
	s_nop 1
	v_cndmask_b32_e32 v4, v3, v4, vcc
	v_mul_lo_u32 v2, v1, v4
	v_add_u32_e32 v1, v2, v1
	s_mov_b64 vcc, exec
	v_mov_b64_e32 v[2:3], s[10:11]
	s_and_saveexec_b64 s[8:9], vcc
	s_cbranch_execz .LBB0_936
	s_add_u32 s10, s4, 0x2400
	s_addc_u32 s11, s5, 0
	v_mov_b32_e32 v4, s98
	v_mov_b32_e32 v1, 0
	global_load_dword v2, v1, s[10:11] sc1
	s_mov_b64 s[16:17], 0
	s_waitcnt vmcnt(0)
	v_cmp_lt_u32_e32 vcc, v2, v4
	s_and_saveexec_b64 s[14:15], vcc
	s_cbranch_execz .LBB0_935
	s_add_u32 s12, s82, 0x4200
	s_addc_u32 s13, s83, 0
	s_mov_b32 s26, 1
	s_branch .LBB0_928

; __device__ __forceinline__ unsigned xb_ld(unsigned* p)              { return __hip_atomic_load(p, __ATOMIC_RELAXED, __HIP_MEMORY_SCOPE_AGENT); }
; __device__ __forceinline__ unsigned xb_add(unsigned* p, unsigned v) { return __hip_atomic_fetch_add(p, v, __ATOMIC_RELAXED, __HIP_MEMORY_SCOPE_AGENT); }
; #define XB_SPIN(cond, bar) do { unsigned _sp = 0; while (cond) { __builtin_amdgcn_s_sleep(1); \
;     if ((++_sp & 255u) == 0u) { if (xb_ld(&(bar)[XB_TMO])) break; if (_sp > XB_SPIN_CAP) { atomicAdd(&(bar)[XB_TMO], 1u); break; } } } } while (0)
; __device__ __forceinline__ void xcd_barrier(const XcdBarrier& b) {
;     ...
;         const unsigned old = xb_add(&bar[XB_XSUB(b.x)], 1u);
;         const unsigned gen = old / nloc;
;         if (old + 1u == (gen + 1u) * nloc) {
;             asm volatile("buffer_inv sc1" ::: "memory");
;             __builtin_amdgcn_fence(__ATOMIC_RELEASE, "agent");
;             asm volatile("s_waitcnt vmcnt(0)" ::: "memory");
;             const unsigned og = xb_add(&bar[XB_TOP], 1u);
;             const unsigned tg = og / nx;
;             if (og + 1u == (tg + 1u) * nx) xb_add(&bar[XB_TOPGEN], 1u);
;             else XB_SPIN(xb_ld(&bar[XB_TOPGEN]) == tg, bar);
;             asm volatile("" ::: "memory");
;             xb_add(&bar[XB_XGEN(b.x)], 1u);
;             asm volatile("" ::: "memory");
;         } else {
;             asm volatile("buffer_inv sc1" ::: "memory");
;             XB_SPIN(xb_ld(&bar[XB_XGEN(b.x)]) == gen, bar);
;             asm volatile("" ::: "memory");
;             asm volatile("s_waitcnt vmcnt(0)" ::: "memory");
;         }
.LBB0_1020:
	s_or_b64 exec, exec, s[12:13]
	v_cvt_f32_u32_e32 v5, v3
	s_waitcnt vmcnt(0)
	v_readfirstlane_b32 s10, v4
	v_sub_u32_e32 v4, 0, v3
	v_rcp_iflag_f32_e32 v5, v5
	v_add_u32_e32 v6, s10, v2
	v_mul_f32_e32 v5, 0x4f7ffffe, v5
	v_cvt_u32_f32_e32 v5, v5
	v_mul_lo_u32 v2, v4, v5
	v_mul_hi_u32 v2, v5, v2
	v_add_u32_e32 v2, v5, v2
	v_mul_hi_u32 v2, v6, v2
	v_mul_lo_u32 v4, v2, v3
	v_sub_u32_e32 v4, v6, v4
	v_add_u32_e32 v5, 1, v2
	v_cmp_ge_u32_e32 vcc, v4, v3
	s_nop 1
	v_cndmask_b32_e32 v2, v2, v5, vcc
	v_sub_u32_e32 v5, v4, v3
	v_cndmask_b32_e32 v4, v4, v5, vcc
	v_add_u32_e32 v5, 1, v2
	v_cmp_ge_u32_e32 vcc, v4, v3
	v_add_u32_e32 v4, 1, v6
	s_nop 0
	v_cndmask_b32_e32 v2, v2, v5, vcc
	v_mul_lo_u32 v5, v3, v2
	v_add_u32_e32 v7, 1, v2
	v_mul_lo_u32 v7, v7, v1
	v_add_u32_e32 v7, v7, v2
	v_add_u32_e32 v3, v5, v3
	v_readfirstlane_b32 s98, v7
	v_cmp_ne_u32_e32 vcc, v4, v3
	s_and_saveexec_b64 s[10:11], vcc
	s_xor_b64 s[10:11], exec, s[10:11]
	s_cbranch_execz .LBB0_1034
	buffer_inv sc1
	v_mov_b32_e32 v2, s98
	s_waitcnt lgkmcnt(0)
	v_mov_b32_e32 v1, 0x2000
	global_load_dword v1, v1, s[8:9] offset:1024 sc1
	s_add_u32 s16, s8, 0x2400
	s_addc_u32 s17, s9, 0
	s_waitcnt vmcnt(0)
	v_cmp_lt_u32_e32 vcc, v1, v2
	s_and_saveexec_b64 s[12:13], vcc
	s_cbranch_execz .LBB0_1033
	s_add_u32 s14, s82, 0x4200
	s_addc_u32 s15, s83, 0
	s_mov_b32 s28, 1
	s_mov_b64 s[18:19], 0
	v_mov_b32_e32 v1, 0
	s_branch .LBB0_1024

; __device__ __forceinline__ unsigned xb_ld(unsigned* p)              { return __hip_atomic_load(p, __ATOMIC_RELAXED, __HIP_MEMORY_SCOPE_AGENT); }
; __device__ __forceinline__ unsigned xb_add(unsigned* p, unsigned v) { return __hip_atomic_fetch_add(p, v, __ATOMIC_RELAXED, __HIP_MEMORY_SCOPE_AGENT); }
; #define XB_SPIN(cond, bar) do { unsigned _sp = 0; while (cond) { __builtin_amdgcn_s_sleep(1); \
;     if ((++_sp & 255u) == 0u) { if (xb_ld(&(bar)[XB_TMO])) break; if (_sp > XB_SPIN_CAP) { atomicAdd(&(bar)[XB_TMO], 1u); break; } } } } while (0)
; __device__ __forceinline__ void xcd_barrier(const XcdBarrier& b) {
;     ...
;             asm volatile("buffer_inv sc1" ::: "memory");
;             __builtin_amdgcn_fence(__ATOMIC_RELEASE, "agent");
;             asm volatile("s_waitcnt vmcnt(0)" ::: "memory");
;             const unsigned og = xb_add(&bar[XB_TOP], 1u);
;             const unsigned tg = og / nx;
;             if (og + 1u == (tg + 1u) * nx) xb_add(&bar[XB_TOPGEN], 1u);
;             else XB_SPIN(xb_ld(&bar[XB_TOPGEN]) == tg, bar);
;             asm volatile("" ::: "memory");
;             xb_add(&bar[XB_XGEN(b.x)], 1u);
;             asm volatile("" ::: "memory");
.LBB0_1034:
	s_andn2_saveexec_b64 s[10:11], s[10:11]
	s_cbranch_execz .LBB0_1054
	s_mov_b64 s[10:11], exec
	buffer_inv sc1
	buffer_wbl2 sc1
	s_waitcnt vmcnt(0) lgkmcnt(0)
	s_waitcnt vmcnt(0)
	v_mbcnt_lo_u32_b32 v2, s10, 0
	v_mbcnt_hi_u32_b32 v2, s11, v2
	v_cmp_eq_u32_e32 vcc, 0, v2
	s_and_saveexec_b64 s[12:13], vcc
	s_cbranch_execz .LBB0_1037
	s_bcnt1_i32_b64 s10, s[10:11]
	v_mov_b32_e32 v3, 0x7000
	v_mov_b32_e32 v4, s10
	v_mov_b32_e32 v3, 0x6400
	global_atomic_add v3, v4, s[82:83]
	global_atomic_add v3, v4, s[82:83] offset:256
	global_atomic_add v3, v4, s[82:83] offset:512
	global_atomic_add v3, v4, s[82:83] offset:768
	global_atomic_add v3, v4, s[82:83] offset:1024
	global_atomic_add v3, v4, s[82:83] offset:1280
	global_atomic_add v3, v4, s[82:83] offset:1536
	global_atomic_add v3, v4, s[82:83] offset:1792
	global_atomic_add v3, v4, s[82:83] offset:2048
	global_atomic_add v3, v4, s[82:83] offset:2304
	global_atomic_add v3, v4, s[82:83] offset:2560
	global_atomic_add v3, v4, s[82:83] offset:2816
	global_atomic_add v3, v4, s[82:83] offset:3072
	global_atomic_add v3, v4, s[82:83] offset:3328
	global_atomic_add v3, v4, s[82:83] offset:3584
	global_atomic_add v3, v4, s[82:83] offset:3840
.LBB0_1037:
	s_or_b64 exec, exec, s[12:13]
	v_cvt_f32_u32_e32 v4, v1
	s_nop 0
	v_readfirstlane_b32 s10, v3
	s_add_u32 s12, s82, 0x7500
	s_addc_u32 s13, s83, 0
	v_rcp_iflag_f32_e32 v4, v4
	v_add_u32_e32 v2, s10, v2
	v_add_u32_e32 v5, 1, v2
	s_mov_b64 s[14:15], -1
	v_mul_f32_e32 v3, 0x4f7ffffe, v4
	v_cvt_u32_f32_e32 v3, v3
	v_sub_u32_e32 v4, 0, v1
	v_mul_lo_u32 v4, v4, v3
	v_mul_hi_u32 v4, v3, v4
	v_add_u32_e32 v3, v3, v4
	v_mul_hi_u32 v3, v2, v3
	v_mul_lo_u32 v4, v3, v1
	v_sub_u32_e32 v2, v2, v4
	v_add_u32_e32 v6, 1, v3
	v_cmp_ge_u32_e32 vcc, v2, v1
	v_sub_u32_e32 v4, v2, v1
	s_nop 0
	v_cndmask_b32_e32 v3, v3, v6, vcc
	v_cndmask_b32_e32 v2, v2, v4, vcc
	v_add_u32_e32 v4, 1, v3
	v_cmp_ge_u32_e32 vcc, v2, v1
	s_nop 1
	v_cndmask_b32_e32 v4, v3, v4, vcc
	v_mul_lo_u32 v2, v1, v4
	v_add_u32_e32 v1, v2, v1
	s_mov_b64 vcc, exec
	v_mov_b64_e32 v[2:3], s[12:13]
	s_and_saveexec_b64 s[10:11], vcc
	s_cbranch_execz .LBB0_1049
	s_add_u32 s12, s8, 0x2400
	s_addc_u32 s13, s9, 0
	v_mov_b32_e32 v4, s98
	v_mov_b32_e32 v1, 0
	global_load_dword v2, v1, s[12:13] sc1
	s_mov_b64 s[18:19], 0
	s_waitcnt vmcnt(0)
	v_cmp_lt_u32_e32 vcc, v2, v4
	s_and_saveexec_b64 s[16:17], vcc
	s_cbranch_execz .LBB0_1048
	s_add_u32 s14, s82, 0x4200
	s_addc_u32 s15, s83, 0
	s_mov_b32 s28, 1
	s_branch .LBB0_1041

; __device__ __forceinline__ unsigned xb_ld(unsigned* p)              { return __hip_atomic_load(p, __ATOMIC_RELAXED, __HIP_MEMORY_SCOPE_AGENT); }
; __device__ __forceinline__ unsigned xb_add(unsigned* p, unsigned v) { return __hip_atomic_fetch_add(p, v, __ATOMIC_RELAXED, __HIP_MEMORY_SCOPE_AGENT); }
; #define XB_SPIN(cond, bar) do { unsigned _sp = 0; while (cond) { __builtin_amdgcn_s_sleep(1); \
;     if ((++_sp & 255u) == 0u) { if (xb_ld(&(bar)[XB_TMO])) break; if (_sp > XB_SPIN_CAP) { atomicAdd(&(bar)[XB_TMO], 1u); break; } } } } while (0)
; __device__ __forceinline__ void xcd_barrier(const XcdBarrier& b) {
;     ...
;         const unsigned old = xb_add(&bar[XB_XSUB(b.x)], 1u);
;         const unsigned gen = old / nloc;
;         if (old + 1u == (gen + 1u) * nloc) {
;             asm volatile("buffer_inv sc1" ::: "memory");
;             __builtin_amdgcn_fence(__ATOMIC_RELEASE, "agent");
;             asm volatile("s_waitcnt vmcnt(0)" ::: "memory");
;             const unsigned og = xb_add(&bar[XB_TOP], 1u);
;             const unsigned tg = og / nx;
;             if (og + 1u == (tg + 1u) * nx) xb_add(&bar[XB_TOPGEN], 1u);
;             else XB_SPIN(xb_ld(&bar[XB_TOPGEN]) == tg, bar);
;             asm volatile("" ::: "memory");
;             xb_add(&bar[XB_XGEN(b.x)], 1u);
;             asm volatile("" ::: "memory");
;         } else {
;             asm volatile("buffer_inv sc1" ::: "memory");
;             XB_SPIN(xb_ld(&bar[XB_XGEN(b.x)]) == gen, bar);
;             asm volatile("" ::: "memory");
;             asm volatile("s_waitcnt vmcnt(0)" ::: "memory");
;         }
.LBB0_1228:
	s_or_b64 exec, exec, s[14:15]
	v_cvt_f32_u32_e32 v5, v3
	s_waitcnt vmcnt(0)
	v_readfirstlane_b32 s12, v4
	v_sub_u32_e32 v4, 0, v3
	v_rcp_iflag_f32_e32 v5, v5
	v_add_u32_e32 v6, s12, v2
	v_mul_f32_e32 v5, 0x4f7ffffe, v5
	v_cvt_u32_f32_e32 v5, v5
	v_mul_lo_u32 v2, v4, v5
	v_mul_hi_u32 v2, v5, v2
	v_add_u32_e32 v2, v5, v2
	v_mul_hi_u32 v2, v6, v2
	v_mul_lo_u32 v4, v2, v3
	v_sub_u32_e32 v4, v6, v4
	v_add_u32_e32 v5, 1, v2
	v_cmp_ge_u32_e32 vcc, v4, v3
	s_nop 1
	v_cndmask_b32_e32 v2, v2, v5, vcc
	v_sub_u32_e32 v5, v4, v3
	v_cndmask_b32_e32 v4, v4, v5, vcc
	v_add_u32_e32 v5, 1, v2
	v_cmp_ge_u32_e32 vcc, v4, v3
	v_add_u32_e32 v4, 1, v6
	s_nop 0
	v_cndmask_b32_e32 v2, v2, v5, vcc
	v_mul_lo_u32 v5, v3, v2
	v_add_u32_e32 v7, 1, v2
	v_mul_lo_u32 v7, v7, v1
	v_add_u32_e32 v7, v7, v2
	v_add_u32_e32 v3, v5, v3
	v_readfirstlane_b32 s98, v7
	v_cmp_ne_u32_e32 vcc, v4, v3
	s_and_saveexec_b64 s[12:13], vcc
	s_xor_b64 s[12:13], exec, s[12:13]
	s_cbranch_execz .LBB0_1242
	buffer_inv sc1
	v_mov_b32_e32 v2, s98
	s_waitcnt lgkmcnt(0)
	v_mov_b32_e32 v1, 0x2000
	global_load_dword v1, v1, s[10:11] offset:1024 sc1
	s_add_u32 s18, s10, 0x2400
	s_addc_u32 s19, s11, 0
	s_waitcnt vmcnt(0)
	v_cmp_lt_u32_e32 vcc, v1, v2
	s_and_saveexec_b64 s[14:15], vcc
	s_cbranch_execz .LBB0_1241
	s_add_u32 s16, s82, 0x4200
	s_addc_u32 s17, s83, 0
	s_mov_b32 s30, 1
	s_mov_b64 s[20:21], 0
	v_mov_b32_e32 v1, 0
	s_branch .LBB0_1232

; __device__ __forceinline__ unsigned xb_ld(unsigned* p)              { return __hip_atomic_load(p, __ATOMIC_RELAXED, __HIP_MEMORY_SCOPE_AGENT); }
; __device__ __forceinline__ unsigned xb_add(unsigned* p, unsigned v) { return __hip_atomic_fetch_add(p, v, __ATOMIC_RELAXED, __HIP_MEMORY_SCOPE_AGENT); }
; #define XB_SPIN(cond, bar) do { unsigned _sp = 0; while (cond) { __builtin_amdgcn_s_sleep(1); \
;     if ((++_sp & 255u) == 0u) { if (xb_ld(&(bar)[XB_TMO])) break; if (_sp > XB_SPIN_CAP) { atomicAdd(&(bar)[XB_TMO], 1u); break; } } } } while (0)
; __device__ __forceinline__ void xcd_barrier(const XcdBarrier& b) {
;     ...
;             asm volatile("buffer_inv sc1" ::: "memory");
;             __builtin_amdgcn_fence(__ATOMIC_RELEASE, "agent");
;             asm volatile("s_waitcnt vmcnt(0)" ::: "memory");
;             const unsigned og = xb_add(&bar[XB_TOP], 1u);
;             const unsigned tg = og / nx;
;             if (og + 1u == (tg + 1u) * nx) xb_add(&bar[XB_TOPGEN], 1u);
;             else XB_SPIN(xb_ld(&bar[XB_TOPGEN]) == tg, bar);
;             asm volatile("" ::: "memory");
;             xb_add(&bar[XB_XGEN(b.x)], 1u);
;             asm volatile("" ::: "memory");
.LBB0_1242:
	s_andn2_saveexec_b64 s[12:13], s[12:13]
	s_cbranch_execz .LBB0_1262
	s_mov_b64 s[12:13], exec
	buffer_inv sc1
	buffer_wbl2 sc1
	s_waitcnt vmcnt(0) lgkmcnt(0)
	s_waitcnt vmcnt(0)
	v_mbcnt_lo_u32_b32 v2, s12, 0
	v_mbcnt_hi_u32_b32 v2, s13, v2
	v_cmp_eq_u32_e32 vcc, 0, v2
	s_and_saveexec_b64 s[14:15], vcc
	s_cbranch_execz .LBB0_1245
	s_bcnt1_i32_b64 s12, s[12:13]
	v_mov_b32_e32 v3, 0x7000
	v_mov_b32_e32 v4, s12
	v_mov_b32_e32 v3, 0x6400
	global_atomic_add v3, v4, s[82:83]
	global_atomic_add v3, v4, s[82:83] offset:256
	global_atomic_add v3, v4, s[82:83] offset:512
	global_atomic_add v3, v4, s[82:83] offset:768
	global_atomic_add v3, v4, s[82:83] offset:1024
	global_atomic_add v3, v4, s[82:83] offset:1280
	global_atomic_add v3, v4, s[82:83] offset:1536
	global_atomic_add v3, v4, s[82:83] offset:1792
	global_atomic_add v3, v4, s[82:83] offset:2048
	global_atomic_add v3, v4, s[82:83] offset:2304
	global_atomic_add v3, v4, s[82:83] offset:2560
	global_atomic_add v3, v4, s[82:83] offset:2816
	global_atomic_add v3, v4, s[82:83] offset:3072
	global_atomic_add v3, v4, s[82:83] offset:3328
	global_atomic_add v3, v4, s[82:83] offset:3584
	global_atomic_add v3, v4, s[82:83] offset:3840
.LBB0_1245:
	s_or_b64 exec, exec, s[14:15]
	v_cvt_f32_u32_e32 v4, v1
	s_nop 0
	v_readfirstlane_b32 s12, v3
	s_add_u32 s14, s82, 0x7500
	s_addc_u32 s15, s83, 0
	v_rcp_iflag_f32_e32 v4, v4
	v_add_u32_e32 v2, s12, v2
	v_add_u32_e32 v5, 1, v2
	s_mov_b64 s[16:17], -1
	v_mul_f32_e32 v3, 0x4f7ffffe, v4
	v_cvt_u32_f32_e32 v3, v3
	v_sub_u32_e32 v4, 0, v1
	v_mul_lo_u32 v4, v4, v3
	v_mul_hi_u32 v4, v3, v4
	v_add_u32_e32 v3, v3, v4
	v_mul_hi_u32 v3, v2, v3
	v_mul_lo_u32 v4, v3, v1
	v_sub_u32_e32 v2, v2, v4
	v_add_u32_e32 v6, 1, v3
	v_cmp_ge_u32_e32 vcc, v2, v1
	v_sub_u32_e32 v4, v2, v1
	s_nop 0
	v_cndmask_b32_e32 v3, v3, v6, vcc
	v_cndmask_b32_e32 v2, v2, v4, vcc
	v_add_u32_e32 v4, 1, v3
	v_cmp_ge_u32_e32 vcc, v2, v1
	s_nop 1
	v_cndmask_b32_e32 v4, v3, v4, vcc
	v_mul_lo_u32 v2, v1, v4
	v_add_u32_e32 v1, v2, v1
	s_mov_b64 vcc, exec
	v_mov_b64_e32 v[2:3], s[14:15]
	s_and_saveexec_b64 s[12:13], vcc
	s_cbranch_execz .LBB0_1257
	s_add_u32 s14, s10, 0x2400
	s_addc_u32 s15, s11, 0
	v_mov_b32_e32 v4, s98
	v_mov_b32_e32 v1, 0
	global_load_dword v2, v1, s[14:15] sc1
	s_mov_b64 s[20:21], 0
	s_waitcnt vmcnt(0)
	v_cmp_lt_u32_e32 vcc, v2, v4
	s_and_saveexec_b64 s[18:19], vcc
	s_cbranch_execz .LBB0_1256
	s_add_u32 s16, s82, 0x4200
	s_addc_u32 s17, s83, 0
	s_mov_b32 s30, 1
	s_branch .LBB0_1249

; __device__ __forceinline__ unsigned xb_ld(unsigned* p)              { return __hip_atomic_load(p, __ATOMIC_RELAXED, __HIP_MEMORY_SCOPE_AGENT); }
; __device__ __forceinline__ unsigned xb_add(unsigned* p, unsigned v) { return __hip_atomic_fetch_add(p, v, __ATOMIC_RELAXED, __HIP_MEMORY_SCOPE_AGENT); }
; #define XB_SPIN(cond, bar) do { unsigned _sp = 0; while (cond) { __builtin_amdgcn_s_sleep(1); \
;     if ((++_sp & 255u) == 0u) { if (xb_ld(&(bar)[XB_TMO])) break; if (_sp > XB_SPIN_CAP) { atomicAdd(&(bar)[XB_TMO], 1u); break; } } } } while (0)
; __device__ __forceinline__ void xcd_barrier(const XcdBarrier& b) {
;     ...
;         const unsigned old = xb_add(&bar[XB_XSUB(b.x)], 1u);
;         const unsigned gen = old / nloc;
;         if (old + 1u == (gen + 1u) * nloc) {
;             asm volatile("buffer_inv sc1" ::: "memory");
;             __builtin_amdgcn_fence(__ATOMIC_RELEASE, "agent");
;             asm volatile("s_waitcnt vmcnt(0)" ::: "memory");
;             const unsigned og = xb_add(&bar[XB_TOP], 1u);
;             const unsigned tg = og / nx;
;             if (og + 1u == (tg + 1u) * nx) xb_add(&bar[XB_TOPGEN], 1u);
;             else XB_SPIN(xb_ld(&bar[XB_TOPGEN]) == tg, bar);
;             asm volatile("" ::: "memory");
;             xb_add(&bar[XB_XGEN(b.x)], 1u);
;             asm volatile("" ::: "memory");
;         } else {
;             asm volatile("buffer_inv sc1" ::: "memory");
;             XB_SPIN(xb_ld(&bar[XB_XGEN(b.x)]) == gen, bar);
;             asm volatile("" ::: "memory");
;             asm volatile("s_waitcnt vmcnt(0)" ::: "memory");
;         }
.LBB0_1841:
	s_or_b64 exec, exec, s[12:13]
	v_cvt_f32_u32_e32 v5, v3
	s_waitcnt vmcnt(0)
	v_readfirstlane_b32 s3, v4
	v_sub_u32_e32 v4, 0, v3
	v_rcp_iflag_f32_e32 v5, v5
	v_add_u32_e32 v6, s3, v2
	v_mul_f32_e32 v5, 0x4f7ffffe, v5
	v_cvt_u32_f32_e32 v5, v5
	v_mul_lo_u32 v2, v4, v5
	v_mul_hi_u32 v2, v5, v2
	v_add_u32_e32 v2, v5, v2
	v_mul_hi_u32 v2, v6, v2
	v_mul_lo_u32 v4, v2, v3
	v_sub_u32_e32 v4, v6, v4
	v_add_u32_e32 v5, 1, v2
	v_cmp_ge_u32_e32 vcc, v4, v3
	s_nop 1
	v_cndmask_b32_e32 v2, v2, v5, vcc
	v_sub_u32_e32 v5, v4, v3
	v_cndmask_b32_e32 v4, v4, v5, vcc
	v_add_u32_e32 v5, 1, v2
	v_cmp_ge_u32_e32 vcc, v4, v3
	v_add_u32_e32 v4, 1, v6
	s_nop 0
	v_cndmask_b32_e32 v2, v2, v5, vcc
	v_mul_lo_u32 v5, v3, v2
	v_add_u32_e32 v7, 1, v2
	v_mul_lo_u32 v7, v7, v1
	v_add_u32_e32 v7, v7, v2
	v_add_u32_e32 v3, v5, v3
	v_readfirstlane_b32 s98, v7
	v_cmp_ne_u32_e32 vcc, v4, v3
	s_and_saveexec_b64 s[10:11], vcc
	s_xor_b64 s[10:11], exec, s[10:11]
	s_cbranch_execz .LBB0_1855
	buffer_inv sc1
	v_mov_b32_e32 v2, s98
	s_waitcnt lgkmcnt(0)
	v_mov_b32_e32 v1, 0x2000
	global_load_dword v1, v1, s[8:9] offset:1024 sc1
	s_add_u32 s16, s8, 0x2400
	s_addc_u32 s17, s9, 0
	s_waitcnt vmcnt(0)
	v_cmp_lt_u32_e32 vcc, v1, v2
	s_and_saveexec_b64 s[12:13], vcc
	s_cbranch_execz .LBB0_1854
	s_add_u32 s14, s82, 0x4200
	s_addc_u32 s15, s83, 0
	s_mov_b32 s3, 1
	s_mov_b64 s[18:19], 0
	v_mov_b32_e32 v1, 0
	s_branch .LBB0_1845

; __device__ __forceinline__ unsigned xb_ld(unsigned* p)              { return __hip_atomic_load(p, __ATOMIC_RELAXED, __HIP_MEMORY_SCOPE_AGENT); }
; __device__ __forceinline__ unsigned xb_add(unsigned* p, unsigned v) { return __hip_atomic_fetch_add(p, v, __ATOMIC_RELAXED, __HIP_MEMORY_SCOPE_AGENT); }
; #define XB_SPIN(cond, bar) do { unsigned _sp = 0; while (cond) { __builtin_amdgcn_s_sleep(1); \
;     if ((++_sp & 255u) == 0u) { if (xb_ld(&(bar)[XB_TMO])) break; if (_sp > XB_SPIN_CAP) { atomicAdd(&(bar)[XB_TMO], 1u); break; } } } } while (0)
; __device__ __forceinline__ void xcd_barrier(const XcdBarrier& b) {
;     ...
;             asm volatile("buffer_inv sc1" ::: "memory");
;             __builtin_amdgcn_fence(__ATOMIC_RELEASE, "agent");
;             asm volatile("s_waitcnt vmcnt(0)" ::: "memory");
;             const unsigned og = xb_add(&bar[XB_TOP], 1u);
;             const unsigned tg = og / nx;
;             if (og + 1u == (tg + 1u) * nx) xb_add(&bar[XB_TOPGEN], 1u);
;             else XB_SPIN(xb_ld(&bar[XB_TOPGEN]) == tg, bar);
;             asm volatile("" ::: "memory");
;             xb_add(&bar[XB_XGEN(b.x)], 1u);
;             asm volatile("" ::: "memory");
.LBB0_1855:
	s_andn2_saveexec_b64 s[10:11], s[10:11]
	s_cbranch_execz .LBB0_1875
	s_mov_b64 s[10:11], exec
	buffer_inv sc1
	buffer_wbl2 sc1
	s_waitcnt vmcnt(0) lgkmcnt(0)
	s_waitcnt vmcnt(0)
	v_mbcnt_lo_u32_b32 v2, s10, 0
	v_mbcnt_hi_u32_b32 v2, s11, v2
	v_cmp_eq_u32_e32 vcc, 0, v2
	s_and_saveexec_b64 s[12:13], vcc
	s_cbranch_execz .LBB0_1858
	s_bcnt1_i32_b64 s3, s[10:11]
	v_mov_b32_e32 v3, 0x7000
	v_mov_b32_e32 v4, s3
	v_mov_b32_e32 v3, 0x6400
	global_atomic_add v3, v4, s[82:83]
	global_atomic_add v3, v4, s[82:83] offset:256
	global_atomic_add v3, v4, s[82:83] offset:512
	global_atomic_add v3, v4, s[82:83] offset:768
	global_atomic_add v3, v4, s[82:83] offset:1024
	global_atomic_add v3, v4, s[82:83] offset:1280
	global_atomic_add v3, v4, s[82:83] offset:1536
	global_atomic_add v3, v4, s[82:83] offset:1792
	global_atomic_add v3, v4, s[82:83] offset:2048
	global_atomic_add v3, v4, s[82:83] offset:2304
	global_atomic_add v3, v4, s[82:83] offset:2560
	global_atomic_add v3, v4, s[82:83] offset:2816
	global_atomic_add v3, v4, s[82:83] offset:3072
	global_atomic_add v3, v4, s[82:83] offset:3328
	global_atomic_add v3, v4, s[82:83] offset:3584
	global_atomic_add v3, v4, s[82:83] offset:3840
.LBB0_1858:
	s_or_b64 exec, exec, s[12:13]
	v_cvt_f32_u32_e32 v4, v1
	s_nop 0
	v_readfirstlane_b32 s3, v3
	s_add_u32 s12, s82, 0x7500
	s_addc_u32 s13, s83, 0
	v_rcp_iflag_f32_e32 v4, v4
	v_add_u32_e32 v2, s3, v2
	v_add_u32_e32 v5, 1, v2
	s_mov_b64 s[14:15], -1
	v_mul_f32_e32 v3, 0x4f7ffffe, v4
	v_cvt_u32_f32_e32 v3, v3
	v_sub_u32_e32 v4, 0, v1
	v_mul_lo_u32 v4, v4, v3
	v_mul_hi_u32 v4, v3, v4
	v_add_u32_e32 v3, v3, v4
	v_mul_hi_u32 v3, v2, v3
	v_mul_lo_u32 v4, v3, v1
	v_sub_u32_e32 v2, v2, v4
	v_add_u32_e32 v6, 1, v3
	v_cmp_ge_u32_e32 vcc, v2, v1
	v_sub_u32_e32 v4, v2, v1
	s_nop 0
	v_cndmask_b32_e32 v3, v3, v6, vcc
	v_cndmask_b32_e32 v2, v2, v4, vcc
	v_add_u32_e32 v4, 1, v3
	v_cmp_ge_u32_e32 vcc, v2, v1
	s_nop 1
	v_cndmask_b32_e32 v4, v3, v4, vcc
	v_mul_lo_u32 v2, v1, v4
	v_add_u32_e32 v1, v2, v1
	s_mov_b64 vcc, exec
	v_mov_b64_e32 v[2:3], s[12:13]
	s_and_saveexec_b64 s[10:11], vcc
	s_cbranch_execz .LBB0_1870
	s_add_u32 s12, s8, 0x2400
	s_addc_u32 s13, s9, 0
	v_mov_b32_e32 v4, s98
	v_mov_b32_e32 v1, 0
	global_load_dword v2, v1, s[12:13] sc1
	s_mov_b64 s[18:19], 0
	s_waitcnt vmcnt(0)
	v_cmp_lt_u32_e32 vcc, v2, v4
	s_and_saveexec_b64 s[16:17], vcc
	s_cbranch_execz .LBB0_1869
	s_add_u32 s14, s82, 0x4200
	s_addc_u32 s15, s83, 0
	s_mov_b32 s3, 1
	s_branch .LBB0_1862
